# baseline (speedup 1.0000x reference)
_Z5k0_lnPKfS0_S0_S0_PDF16_S1_S1_S0_S0_S0_S0_S0_S0_S0_S1_:
	s_cmpk_lt_u32 s2, 0x400
	s_mov_b64 s[4:5], -1
	s_cbranch_scc0 .LBB0_4
	s_load_dwordx8 s[4:11], s[0:1], 0x0
	s_lshr_b32 s18, s2, 8
	s_lshl_b32 s3, s2, 6
	s_mov_b32 s19, 0
	s_and_b32 s20, s3, 0x3fc0
	s_lshl_b64 s[22:23], s[18:19], 22
	s_waitcnt lgkmcnt(0)
	v_lshrrev_b32_e32 v70, 3, v0
	v_lshlrev_b32_e32 v70, 2, v70
	v_and_b32_e32 v71, 7, v0
	v_lshlrev_b32_e32 v71, 5, v71
	global_load_dword v72, v70, s[8:9]
	global_load_dword v74, v70, s[10:11]
	global_load_dword v76, v70, s[8:9] offset:128
	global_load_dword v78, v70, s[10:11] offset:128
	global_load_dwordx4 v[80:83], v71, s[8:9] offset:16
	global_load_dwordx4 v[84:87], v71, s[8:9]
	global_load_dwordx4 v[88:91], v71, s[10:11] offset:16
	global_load_dwordx4 v[92:95], v71, s[10:11]
	s_add_u32 s3, s4, s22
	s_addc_u32 s5, s5, s23
	s_lshl_b32 s24, s20, 2
	s_add_u32 s4, s3, s24
	v_lshlrev_b32_e32 v2, 4, v0
	s_addc_u32 s5, s5, 0
	v_lshlrev_b32_e32 v1, 10, v0
	v_and_b32_e32 v30, 0xf0, v2
	v_mov_b32_e32 v31, 0
	v_lshlrev_b32_e32 v4, 12, v0
	s_mov_b32 s3, 0x7c000
	v_mov_b32_e32 v8, 0x40000
	v_lshl_add_u64 v[2:3], s[4:5], 0, v[30:31]
	v_and_b32_e32 v4, 0xf0000, v4
	v_mov_b32_e32 v5, v31
	v_bitop3_b32 v8, v1, s3, v8 bitop3:0xc8
	v_lshl_add_u64 v[6:7], v[2:3], 0, v[4:5]
	v_lshlrev_b32_e32 v8, 2, v8
	v_mov_b32_e32 v9, v31
	v_lshl_add_u64 v[10:11], v[2:3], 0, v[8:9]
	global_load_dwordx4 v[20:23], v[6:7], off nt
	global_load_dwordx4 v[24:27], v[10:11], off nt
	s_mov_b32 s3, 0xbc000
	v_mov_b32_e32 v6, 0x80000
	v_bitop3_b32 v6, v1, s3, v6 bitop3:0xc8
	v_lshlrev_b32_e32 v6, 2, v6
	v_mov_b32_e32 v7, v31
	v_lshl_add_u64 v[10:11], v[2:3], 0, v[6:7]
	global_load_dwordx4 v[32:35], v[10:11], off nt
	s_mov_b32 s3, 0xfc000
	v_mov_b32_e32 v10, 0xc0000
	v_bitop3_b32 v1, v1, s3, v10 bitop3:0xc8
	v_lshlrev_b32_e32 v10, 2, v1
	v_mov_b32_e32 v11, v31
	v_lshl_add_u64 v[2:3], v[2:3], 0, v[10:11]
	global_load_dwordx4 v[36:39], v[2:3], off nt
	s_add_u32 s4, s6, s22
	s_addc_u32 s5, s7, s23
	v_or_b32_e32 v3, 0x200, v0
	s_add_u32 s4, s4, s24
	v_lshrrev_b32_e32 v2, 4, v0
	s_movk_i32 s3, 0x104
	v_lshrrev_b32_e32 v3, 4, v3
	s_addc_u32 s5, s5, 0
	v_or_b32_e32 v18, 0x100, v0
	v_or_b32_e32 v12, 0x300, v0
	v_and_b32_e32 v13, 63, v0
	v_lshrrev_b32_e32 v45, 2, v0
	v_mul_u32_u24_e32 v1, 0x104, v2
	v_mad_u32_u24 v51, v2, s3, v30
	v_mul_u32_u24_e32 v43, 0x104, v3
	v_mad_u32_u24 v53, v3, s3, v30
	v_lshl_add_u64 v[2:3], s[4:5], 0, v[30:31]
	v_lshrrev_b32_e32 v14, 4, v18
	v_lshrrev_b32_e32 v50, 4, v12
	v_and_b32_e32 v12, 48, v45
	v_lshlrev_b32_e32 v19, 2, v13
	v_lshl_add_u64 v[68:69], v[2:3], 0, v[4:5]
	s_load_dwordx4 s[12:15], s[0:1], 0x20
	s_load_dwordx2 s[16:17], s[0:1], 0x30
	v_mul_u32_u24_e32 v44, 0x104, v14
	v_mad_u32_u24 v52, v14, s3, v30
	v_mad_u32_u24 v55, v12, s3, v19
	v_lshl_add_u64 v[40:41], v[2:3], 0, v[8:9]
	v_lshl_add_u64 v[46:47], v[2:3], 0, v[6:7]
	v_lshl_add_u64 v[48:49], v[2:3], 0, v[10:11]
	v_mad_u32_u24 v54, v50, s3, v30
	v_add_u32_e32 v56, 0x400, v55
	v_add_u32_e32 v28, 0x800, v55
	v_lshlrev_b32_e32 v42, 2, v0
	s_mov_b32 s21, s19
	v_cmp_gt_u32_e32 vcc, 64, v0
	s_waitcnt vmcnt(3)
	ds_write2_b32 v51, v20, v21 offset1:1
	ds_write2_b32 v51, v22, v23 offset0:2 offset1:3
	s_waitcnt vmcnt(2)
	ds_write2_b32 v52, v24, v25 offset1:1
	ds_write2_b32 v52, v26, v27 offset0:2 offset1:3
	s_waitcnt vmcnt(1)
	ds_write2_b32 v53, v32, v33 offset1:1
	ds_write2_b32 v53, v34, v35 offset0:2 offset1:3
	s_waitcnt vmcnt(0)
	ds_write2_b32 v54, v36, v37 offset1:1
	ds_write2_b32 v54, v38, v39 offset0:2 offset1:3
	s_waitcnt lgkmcnt(0)
	s_barrier
	global_load_dwordx4 v[14:17], v[68:69], off nt
	global_load_dwordx4 v[10:13], v[40:41], off nt
	global_load_dwordx4 v[6:9], v[46:47], off nt
	global_load_dwordx4 v[2:5], v[48:49], off nt
	ds_read2_b32 v[20:21], v55 offset1:65
	ds_read2_b32 v[22:23], v55 offset0:130 offset1:195
	ds_read2_b32 v[24:25], v56 offset0:4 offset1:69
	ds_read2_b32 v[26:27], v56 offset0:134 offset1:199
	s_waitcnt lgkmcnt(3)
	v_add_f32_e32 v20, 0, v20
	v_add_f32_e32 v20, v20, v21
	s_waitcnt lgkmcnt(2)
	v_add_f32_e32 v20, v20, v22
	v_add_f32_e32 v20, v20, v23
	s_waitcnt lgkmcnt(1)
	v_add_f32_e32 v22, v20, v24
	ds_read2_b32 v[20:21], v28 offset0:8 offset1:73
	v_add_f32_e32 v24, v22, v25
	ds_read2_b32 v[22:23], v28 offset0:138 offset1:203
	s_waitcnt lgkmcnt(2)
	v_add_f32_e32 v24, v24, v26
	v_add_f32_e32 v24, v24, v27
	s_waitcnt lgkmcnt(1)
	v_add_f32_e32 v20, v24, v20
	v_add_f32_e32 v20, v20, v21
	v_add_u32_e32 v26, 0xc00, v55
	s_waitcnt lgkmcnt(0)
	v_add_f32_e32 v22, v20, v22
	ds_read2_b32 v[20:21], v26 offset0:12 offset1:77
	v_or_b32_e32 v24, 15, v45
	v_mad_u32_u24 v27, v24, s3, v19
	ds_read_b32 v24, v55 offset:3640
	ds_read_b32 v25, v27
	v_add_f32_e32 v22, v22, v23
	s_waitcnt lgkmcnt(2)
	v_add_f32_e32 v20, v22, v20
	v_add_f32_e32 v20, v20, v21
	s_waitcnt lgkmcnt(1)
	v_add_f32_e32 v20, v20, v24
	s_waitcnt lgkmcnt(0)
	v_add_f32_e32 v20, v20, v25
	ds_write_b32 v42, v20 offset:16640
	s_waitcnt lgkmcnt(0)
	s_barrier
	ds_read2st64_b32 v[20:21], v19 offset0:65 offset1:66
	ds_read2st64_b32 v[22:23], v19 offset0:67 offset1:68
	s_waitcnt lgkmcnt(0)
	s_barrier
	ds_read2_b32 v[24:25], v55 offset1:65
	v_add_f32_e32 v20, v20, v21
	v_add_f32_e32 v20, v20, v22
	v_add_f32_e32 v20, v20, v23
	ds_read2_b32 v[22:23], v55 offset0:130 offset1:195
	s_waitcnt lgkmcnt(1)
	v_fmac_f32_e32 v25, 0xbc800000, v20
	v_fmamk_f32 v21, v20, 0xbc800000, v24
	v_mul_f32_e32 v29, v25, v25
	ds_read2_b32 v[24:25], v56 offset0:4 offset1:69
	v_fmac_f32_e32 v29, v21, v21
	s_waitcnt lgkmcnt(1)
	v_fmamk_f32 v21, v20, 0xbc800000, v22
	v_fmac_f32_e32 v29, v21, v21
	v_fmac_f32_e32 v23, 0xbc800000, v20
	v_fmac_f32_e32 v29, v23, v23
	s_waitcnt lgkmcnt(0)
	v_fmamk_f32 v21, v20, 0xbc800000, v24
	ds_read2_b32 v[22:23], v56 offset0:134 offset1:199
	v_fmac_f32_e32 v29, v21, v21
	v_fmac_f32_e32 v25, 0xbc800000, v20
	v_fmac_f32_e32 v29, v25, v25
	ds_read2_b32 v[24:25], v28 offset0:8 offset1:73
	s_waitcnt lgkmcnt(1)
	v_fmamk_f32 v21, v20, 0xbc800000, v22
	v_fmac_f32_e32 v29, v21, v21
	v_fmac_f32_e32 v23, 0xbc800000, v20
	v_fmac_f32_e32 v29, v23, v23
	s_waitcnt lgkmcnt(0)
	v_fmamk_f32 v21, v20, 0xbc800000, v24
	ds_read2_b32 v[22:23], v28 offset0:138 offset1:203
	v_fmac_f32_e32 v29, v21, v21
	v_fmac_f32_e32 v25, 0xbc800000, v20
	v_fmac_f32_e32 v29, v25, v25
	ds_read2_b32 v[24:25], v26 offset0:12 offset1:77
	s_waitcnt lgkmcnt(1)
	v_fmamk_f32 v21, v20, 0xbc800000, v22
	v_fmac_f32_e32 v29, v21, v21
	v_fmac_f32_e32 v23, 0xbc800000, v20
	v_fmac_f32_e32 v29, v23, v23
	s_waitcnt lgkmcnt(0)
	v_fmamk_f32 v21, v20, 0xbc800000, v24
	ds_read_b32 v22, v55 offset:3640
	v_fmac_f32_e32 v29, v21, v21
	ds_read_b32 v21, v27
	v_fmac_f32_e32 v25, 0xbc800000, v20
	v_fmac_f32_e32 v29, v25, v25
	s_waitcnt lgkmcnt(1)
	v_fmac_f32_e32 v22, 0xbc800000, v20
	v_fmac_f32_e32 v29, v22, v22
	s_waitcnt lgkmcnt(0)
	v_fmac_f32_e32 v21, 0xbc800000, v20
	v_mul_u32_u24_e32 v45, 0x104, v50
	v_fmac_f32_e32 v29, v21, v21
	ds_write_b32 v42, v29 offset:16640
	s_waitcnt lgkmcnt(0)
	s_barrier
	s_and_saveexec_b64 s[6:7], vcc
	s_cbranch_execz .LBB0_3
	v_or_b32_e32 v21, 0x4100, v19
	ds_read2st64_b32 v[22:23], v21 offset1:1
	ds_read2st64_b32 v[24:25], v21 offset0:2 offset1:3
	v_mov_b32_e32 v21, 0x3727c5ac
	s_mov_b32 s4, 0xf800000
	v_mul_f32_e32 v20, 0x3c800000, v20
	s_waitcnt lgkmcnt(1)
	v_add_f32_e32 v22, v22, v23
	s_waitcnt lgkmcnt(0)
	v_add_f32_e32 v22, v22, v24
	v_add_f32_e32 v22, v22, v25
	v_fmac_f32_e32 v21, 0x3c800000, v22
	v_mul_f32_e32 v22, 0x4f800000, v21
	v_cmp_gt_f32_e32 vcc, s4, v21
	s_nop 1
	v_cndmask_b32_e32 v21, v21, v22, vcc
	v_sqrt_f32_e32 v22, v21
	s_nop 0
	v_add_u32_e32 v23, -1, v22
	v_add_u32_e32 v24, 1, v22
	v_fma_f32 v25, -v23, v22, v21
	v_fma_f32 v26, -v24, v22, v21
	v_cmp_ge_f32_e64 s[4:5], 0, v25
	s_nop 1
	v_cndmask_b32_e64 v22, v22, v23, s[4:5]
	v_cmp_lt_f32_e64 s[4:5], 0, v26
	s_nop 1
	v_cndmask_b32_e64 v22, v22, v24, s[4:5]
	v_mul_f32_e32 v23, 0x37800000, v22
	v_cndmask_b32_e32 v22, v22, v23, vcc
	v_mov_b32_e32 v23, 0x260
	v_cmp_class_f32_e32 vcc, v21, v23
	s_nop 1
	v_cndmask_b32_e32 v21, v22, v21, vcc
	v_div_scale_f32 v22, s[4:5], v21, v21, 1.0
	v_rcp_f32_e32 v23, v22
	s_nop 0
	v_fma_f32 v24, -v22, v23, 1.0
	v_fmac_f32_e32 v23, v24, v23
	v_div_scale_f32 v24, vcc, 1.0, v21, 1.0
	v_mul_f32_e32 v25, v24, v23
	v_fma_f32 v26, -v22, v25, v24
	v_fmac_f32_e32 v25, v26, v23
	v_fma_f32 v22, -v22, v25, v24
	v_div_fmas_f32 v22, v22, v23, v25
	v_div_fixup_f32 v21, v22, v21, 1.0
	ds_write2st64_b32 v19, v20, v21 offset0:69 offset1:70
.LBB0_3:
	s_or_b64 exec, exec, s[6:7]
	v_lshrrev_b32_e32 v26, 3, v0
	v_lshlrev_b32_e32 v41, 2, v26
	s_waitcnt lgkmcnt(0)
	s_barrier
	v_lshlrev_b32_e32 v19, 3, v0
	v_and_b32_e32 v28, 56, v19
	v_lshlrev_b32_e32 v61, 2, v28
	v_mad_u32_u24 v19, v26, s3, v61
	ds_read2_b32 v[46:47], v19 offset1:1
	ds_read_b128 v[20:23], v61 offset:17664
	ds_read_b128 v[36:39], v61 offset:17680
	ds_read2_b32 v[52:53], v19 offset0:2 offset1:3
	ds_read2_b32 v[58:59], v19 offset0:6 offset1:7
	s_lshl_b32 s6, s18, 21
	s_waitcnt lgkmcnt(3)
	v_pk_add_f32 v[50:51], v[46:47], v[20:21] neg_lo:[0,1] neg_hi:[0,1]
	ds_read_b128 v[46:49], v61 offset:17920
	s_waitcnt lgkmcnt(2)
	v_pk_add_f32 v[52:53], v[52:53], v[22:23] neg_lo:[0,1] neg_hi:[0,1]
	s_lshl_b32 s4, s20, 1
	s_waitcnt lgkmcnt(1)
	v_pk_add_f32 v[58:59], v[58:59], v[38:39] neg_lo:[0,1] neg_hi:[0,1]
	s_add_u32 s4, s12, s4
	s_waitcnt lgkmcnt(0)
	v_pk_mul_f32 v[50:51], v[50:51], v[46:47]
	v_pk_mul_f32 v[52:53], v[52:53], v[48:49]
	s_addc_u32 s5, s13, 0
	v_lshlrev_b32_e32 v32, 1, v28
	v_mov_b32_e32 v33, v31
	v_lshl_add_u64 v[24:25], s[4:5], 0, v[32:33]
	v_mul_u32_u24_e32 v60, 0x104, v26
	v_mov_b32_e32 v27, v31
	s_lshl_b64 s[4:5], s[18:19], 14
	s_or_b64 s[4:5], s[4:5], s[20:21]
	v_add_u32_e32 v1, v30, v1
	ds_read_b128 v[54:57], v61 offset:17936
	s_waitcnt lgkmcnt(0)
	v_pk_mul_f32 v[58:59], v[58:59], v[56:57]
	s_nop 0
	v_pk_fma_f32 v[50:51], v[72:73], v[50:51], v[74:75] op_sel_hi:[0,1,0]
	v_pk_fma_f32 v[52:53], v[72:73], v[52:53], v[74:75] op_sel_hi:[0,1,0]
	v_cvt_pk_f16_f32 v50, v50, v51
	v_cvt_pk_f16_f32 v51, v52, v53
	ds_read2_b32 v[52:53], v19 offset0:4 offset1:5
	s_waitcnt lgkmcnt(0)
	v_pk_add_f32 v[52:53], v[52:53], v[36:37] neg_lo:[0,1] neg_hi:[0,1]
	s_nop 0
	v_pk_mul_f32 v[52:53], v[52:53], v[54:55]
	s_nop 0
	v_pk_fma_f32 v[52:53], v[72:73], v[52:53], v[74:75] op_sel_hi:[0,1,0]
	v_pk_fma_f32 v[34:35], v[72:73], v[58:59], v[74:75] op_sel_hi:[0,1,0]
	v_cvt_pk_f16_f32 v52, v52, v53
	v_cvt_pk_f16_f32 v53, v34, v35
	v_lshl_or_b32 v34, v26, 15, s6
	v_mov_b32_e32 v35, v31
	v_lshl_add_u64 v[34:35], v[24:25], 0, v[34:35]
	global_store_dwordx4 v[34:35], v[50:53], off
	v_lshrrev_b32_e32 v34, 3, v18
	v_lshlrev_b32_e32 v29, 2, v34
	v_mad_u32_u24 v50, v34, s3, v61
	ds_read2_b32 v[18:19], v50 offset1:1
	v_mov_b32_e32 v35, v31
	s_waitcnt lgkmcnt(0)
	v_pk_add_f32 v[18:19], v[18:19], v[20:21] neg_lo:[0,1] neg_hi:[0,1]
	ds_read2_b32 v[20:21], v50 offset0:2 offset1:3
	v_pk_mul_f32 v[18:19], v[18:19], v[46:47]
	s_waitcnt lgkmcnt(0)
	v_pk_add_f32 v[20:21], v[20:21], v[22:23] neg_lo:[0,1] neg_hi:[0,1]
	s_nop 0
	v_pk_mul_f32 v[20:21], v[20:21], v[48:49]
	ds_read2_b32 v[22:23], v50 offset0:6 offset1:7
	s_waitcnt lgkmcnt(0)
	v_pk_add_f32 v[22:23], v[22:23], v[38:39] neg_lo:[0,1] neg_hi:[0,1]
	ds_read2st64_b32 v[38:39], v41 offset0:69 offset1:70
	v_pk_mul_f32 v[22:23], v[22:23], v[56:57]
	s_nop 0
	v_pk_fma_f32 v[18:19], v[76:77], v[18:19], v[78:79] op_sel_hi:[0,1,0]
	v_pk_fma_f32 v[20:21], v[76:77], v[20:21], v[78:79] op_sel_hi:[0,1,0]
	v_cvt_pk_f16_f32 v18, v18, v19
	v_cvt_pk_f16_f32 v19, v20, v21
	ds_read2_b32 v[20:21], v50 offset0:4 offset1:5
	v_pk_fma_f32 v[22:23], v[76:77], v[22:23], v[78:79] op_sel_hi:[0,1,0]
	s_waitcnt lgkmcnt(0)
	v_pk_add_f32 v[20:21], v[20:21], v[36:37] neg_lo:[0,1] neg_hi:[0,1]
	s_nop 0
	v_pk_mul_f32 v[20:21], v[20:21], v[54:55]
	v_lshl_add_u64 v[36:37], s[14:15], 0, v[32:33]
	v_pk_fma_f32 v[20:21], v[76:77], v[20:21], v[78:79] op_sel_hi:[0,1,0]
	v_cvt_pk_f16_f32 v20, v20, v21
	v_cvt_pk_f16_f32 v21, v22, v23
	v_lshl_or_b32 v22, v34, 15, s6
	v_mov_b32_e32 v23, v31
	v_lshl_add_u64 v[22:23], v[24:25], 0, v[22:23]
	global_store_dwordx4 v[22:23], v[18:21], off
	v_mov_b32_e32 v40, v39
	s_nop 0
	v_lshlrev_b32_e32 v18, 8, v26
	v_sub_u32_e32 v41, v60, v18
	v_mad_u32_u24 v31, v28, s3, v41
	ds_read2_b32 v[18:19], v31 offset1:65
	v_lshl_add_u64 v[26:27], s[4:5], 0, v[26:27]
	s_waitcnt lgkmcnt(0)
	v_pk_add_f32 v[18:19], v[18:19], v[38:39] op_sel_hi:[1,0] neg_lo:[0,1] neg_hi:[0,1]
	s_nop 0
	v_pk_mul_f32 v[46:47], v[40:41], v[18:19] op_sel_hi:[0,1]
	v_mov_b32_e32 v39, 0x208
	v_mad_u32_u24 v64, v28, s3, v39
	s_nop 0
	v_pk_fma_f32 v[46:47], v[84:85], v[46:47], v[92:93]
	s_nop 0
	v_cvt_pk_f16_f32 v60, v46, v47
	v_add_u32_e32 v47, 0x200, v31
	v_add_u32_e32 v46, v41, v64
	ds_read2_b32 v[50:51], v47 offset0:67 offset1:197
	ds_read_b32 v48, v46
	s_waitcnt lgkmcnt(1)
	v_mov_b32_e32 v49, v50
	s_waitcnt lgkmcnt(0)
	v_pk_add_f32 v[48:49], v[48:49], v[38:39] op_sel_hi:[1,0] neg_lo:[0,1] neg_hi:[0,1]
	v_mov_b32_e32 v39, 0x410
	v_pk_mul_f32 v[48:49], v[40:41], v[48:49] op_sel_hi:[0,1]
	v_pk_fma_f32 v[48:49], v[86:87], v[48:49], v[94:95]
	v_mad_u32_u24 v65, v28, s3, v39
	v_cvt_pk_f16_f32 v61, v48, v49
	v_add_u32_e32 v48, v41, v65
	ds_read_b32 v50, v48
	s_waitcnt lgkmcnt(0)
	v_pk_add_f32 v[50:51], v[50:51], v[38:39] op_sel_hi:[1,0] neg_lo:[0,1] neg_hi:[0,1]
	v_mov_b32_e32 v39, 0x618
	v_pk_mul_f32 v[50:51], v[40:41], v[50:51] op_sel_hi:[0,1]
	v_mad_u32_u24 v66, v28, s3, v39
	v_pk_fma_f32 v[50:51], v[80:81], v[50:51], v[88:89]
	v_add_u32_e32 v49, v41, v66
	v_cvt_pk_f16_f32 v62, v50, v51
	ds_read_b32 v50, v49
	ds_read_b32 v51, v31 offset:1820
	s_waitcnt lgkmcnt(0)
	v_pk_add_f32 v[38:39], v[50:51], v[38:39] op_sel_hi:[1,0] neg_lo:[0,1] neg_hi:[0,1]
	s_nop 0
	v_pk_mul_f32 v[38:39], v[40:41], v[38:39] op_sel_hi:[0,1]
	v_pk_fma_f32 v[38:39], v[82:83], v[38:39], v[90:91]
	v_mad_u32_u24 v50, v28, s3, v29
	v_cvt_pk_f16_f32 v63, v38, v39
	v_lshlrev_b64 v[38:39], 7, v[26:27]
	v_lshl_add_u64 v[26:27], v[36:37], 0, v[38:39]
	global_store_dwordx4 v[26:27], v[60:63], off sc1
	ds_read2st64_b32 v[40:41], v29 offset0:69 offset1:70
	ds_read2_b32 v[26:27], v50 offset1:65
	v_add_u32_e32 v51, 0x200, v50
	s_waitcnt lgkmcnt(1)
	v_mov_b32_e32 v42, v41
	s_waitcnt lgkmcnt(0)
	v_pk_add_f32 v[26:27], v[26:27], v[40:41] op_sel_hi:[1,0] neg_lo:[0,1] neg_hi:[0,1]
	v_add_u32_e32 v41, v29, v64
	v_pk_mul_f32 v[26:27], v[42:43], v[26:27] op_sel_hi:[0,1]
	v_pk_fma_f32 v[26:27], v[84:85], v[26:27], v[92:93]
	ds_read2_b32 v[56:57], v51 offset0:67 offset1:197
	ds_read_b32 v52, v41
	v_cvt_pk_f16_f32 v26, v26, v27
	s_waitcnt lgkmcnt(1)
	v_mov_b32_e32 v53, v56
	s_waitcnt lgkmcnt(0)
	v_pk_add_f32 v[52:53], v[52:53], v[40:41] op_sel_hi:[1,0] neg_lo:[0,1] neg_hi:[0,1]
	s_nop 0
	v_pk_mul_f32 v[52:53], v[42:43], v[52:53] op_sel_hi:[0,1]
	v_pk_fma_f32 v[52:53], v[86:87], v[52:53], v[94:95]
	v_add_u32_e32 v54, v29, v65
	ds_read_b32 v56, v54
	v_cvt_pk_f16_f32 v27, v52, v53
	s_waitcnt lgkmcnt(0)
	v_pk_add_f32 v[52:53], v[56:57], v[40:41] op_sel_hi:[1,0] neg_lo:[0,1] neg_hi:[0,1]
	s_nop 0
	v_pk_mul_f32 v[52:53], v[42:43], v[52:53] op_sel_hi:[0,1]
	v_pk_fma_f32 v[18:19], v[80:81], v[52:53], v[88:89]
	v_add_u32_e32 v22, v29, v66
	v_cvt_pk_f16_f32 v28, v18, v19
	ds_read_b32 v18, v22
	ds_read_b32 v19, v50 offset:1820
	s_waitcnt lgkmcnt(0)
	v_pk_add_f32 v[18:19], v[18:19], v[40:41] op_sel_hi:[1,0] neg_lo:[0,1] neg_hi:[0,1]
	s_nop 0
	v_pk_mul_f32 v[18:19], v[42:43], v[18:19] op_sel_hi:[0,1]
	v_pk_fma_f32 v[18:19], v[82:83], v[18:19], v[90:91]
	s_nop 0
	v_cvt_pk_f16_f32 v29, v18, v19
	v_lshl_add_u64 v[18:19], s[4:5], 0, v[34:35]
	v_lshlrev_b64 v[18:19], 7, v[18:19]
	v_lshl_add_u64 v[20:21], v[36:37], 0, v[18:19]
	global_store_dwordx4 v[20:21], v[26:29], off sc1
	s_barrier
	s_waitcnt vmcnt(4)
	ds_write2_b32 v1, v14, v15 offset1:1
	ds_write2_b32 v1, v16, v17 offset0:2 offset1:3
	v_add_u32_e32 v1, v30, v44
	ds_write2_b32 v1, v10, v11 offset1:1
	ds_write2_b32 v1, v12, v13 offset0:2 offset1:3
	v_add_u32_e32 v1, v30, v43
	ds_write2_b32 v1, v6, v7 offset1:1
	ds_write2_b32 v1, v8, v9 offset0:2 offset1:3
	v_add_u32_e32 v1, v30, v45
	ds_write2_b32 v1, v2, v3 offset1:1
	ds_write2_b32 v1, v4, v5 offset0:2 offset1:3
	s_waitcnt lgkmcnt(0)
	s_barrier
	ds_read2_b32 v[8:9], v31 offset1:65
	ds_read_b32 v1, v46
	ds_read2_b32 v[2:3], v47 offset0:67 offset1:197
	ds_read_b32 v4, v48
	ds_read_b32 v5, v49
	ds_read_b32 v10, v31 offset:1820
	v_lshl_add_u64 v[6:7], s[16:17], 0, v[32:33]
	s_mov_b64 s[4:5], 0
	s_waitcnt lgkmcnt(2)
	v_cvt_pk_f16_f32 v4, v4, v3
	v_cvt_pk_f16_f32 v3, v1, v2
	s_waitcnt lgkmcnt(0)
	v_cvt_pk_f16_f32 v5, v5, v10
	v_cvt_pk_f16_f32 v2, v8, v9
	v_lshl_add_u64 v[8:9], v[6:7], 0, v[38:39]
	global_store_dwordx4 v[8:9], v[2:5], off sc1
	ds_read2_b32 v[8:9], v50 offset1:65
	ds_read_b32 v1, v41
	ds_read2_b32 v[2:3], v51 offset0:67 offset1:197
	ds_read_b32 v4, v54
	ds_read_b32 v5, v22
	ds_read_b32 v10, v50 offset:1820
	v_lshl_add_u64 v[6:7], v[6:7], 0, v[18:19]
	s_waitcnt lgkmcnt(2)
	v_cvt_pk_f16_f32 v4, v4, v3
	v_cvt_pk_f16_f32 v3, v1, v2
	s_waitcnt lgkmcnt(0)
	v_cvt_pk_f16_f32 v5, v5, v10
	v_cvt_pk_f16_f32 v2, v8, v9
	global_store_dwordx4 v[6:7], v[2:5], off sc1

	.amdhsa_kernel _Z5k0_lnPKfS0_S0_S0_PDF16_S1_S1_S0_S0_S0_S0_S0_S0_S0_S1_
		.amdhsa_group_segment_fixed_size 18176
		.amdhsa_private_segment_fixed_size 0
		.amdhsa_kernarg_size 120
		.amdhsa_user_sgpr_count 2
		.amdhsa_user_sgpr_dispatch_ptr 0
		.amdhsa_user_sgpr_queue_ptr 0
		.amdhsa_user_sgpr_kernarg_segment_ptr 1
		.amdhsa_user_sgpr_dispatch_id 0
		.amdhsa_user_sgpr_kernarg_preload_length 0
		.amdhsa_user_sgpr_kernarg_preload_offset 0
		.amdhsa_user_sgpr_private_segment_size 0
		.amdhsa_uses_dynamic_stack 0
		.amdhsa_enable_private_segment 0
		.amdhsa_system_sgpr_workgroup_id_x 1
		.amdhsa_system_sgpr_workgroup_id_y 0
		.amdhsa_system_sgpr_workgroup_id_z 0
		.amdhsa_system_sgpr_workgroup_info 0
		.amdhsa_system_vgpr_workitem_id 0
		.amdhsa_next_free_vgpr 96
		.amdhsa_next_free_sgpr 25
		.amdhsa_accum_offset 96
		.amdhsa_reserve_vcc 1
		.amdhsa_float_round_mode_32 0
		.amdhsa_float_round_mode_16_64 0
		.amdhsa_float_denorm_mode_32 3
		.amdhsa_float_denorm_mode_16_64 3
		.amdhsa_dx10_clamp 1
		.amdhsa_ieee_mode 1
		.amdhsa_fp16_overflow 0
		.amdhsa_tg_split 0
		.amdhsa_exception_fp_ieee_invalid_op 0
		.amdhsa_exception_fp_denorm_src 0
		.amdhsa_exception_fp_ieee_div_zero 0
		.amdhsa_exception_fp_ieee_overflow 0
		.amdhsa_exception_fp_ieee_underflow 0
		.amdhsa_exception_fp_ieee_inexact 0
		.amdhsa_exception_int_div_zero 0
	.end_amdhsa_kernel

amdhsa.kernels:
  - .agpr_count:     0
    .args:
      - .actual_access:  read_only
        .address_space:  global
        .offset:         0
        .size:           8
        .value_kind:     global_buffer
      - .actual_access:  read_only
        .address_space:  global
        .offset:         8
        .size:           8
        .value_kind:     global_buffer
      - .actual_access:  read_only
        .address_space:  global
        .offset:         16
        .size:           8
        .value_kind:     global_buffer
      - .actual_access:  read_only
        .address_space:  global
        .offset:         24
        .size:           8
        .value_kind:     global_buffer
      - .actual_access:  write_only
        .address_space:  global
        .offset:         32
        .size:           8
        .value_kind:     global_buffer
      - .actual_access:  write_only
        .address_space:  global
        .offset:         40
        .size:           8
        .value_kind:     global_buffer
      - .actual_access:  write_only
        .address_space:  global
        .offset:         48
        .size:           8
        .value_kind:     global_buffer
      - .actual_access:  read_only
        .address_space:  global
        .offset:         56
        .size:           8
        .value_kind:     global_buffer
      - .actual_access:  read_only
        .address_space:  global
        .offset:         64
        .size:           8
        .value_kind:     global_buffer
      - .actual_access:  read_only
        .address_space:  global
        .offset:         72
        .size:           8
        .value_kind:     global_buffer
      - .actual_access:  read_only
        .address_space:  global
        .offset:         80
        .size:           8
        .value_kind:     global_buffer
      - .actual_access:  read_only
        .address_space:  global
        .offset:         88
        .size:           8
        .value_kind:     global_buffer
      - .actual_access:  read_only
        .address_space:  global
        .offset:         96
        .size:           8
        .value_kind:     global_buffer
      - .actual_access:  read_only
        .address_space:  global
        .offset:         104
        .size:           8
        .value_kind:     global_buffer
      - .actual_access:  write_only
        .address_space:  global
        .offset:         112
        .size:           8
        .value_kind:     global_buffer
    .group_segment_fixed_size: 18176
    .kernarg_segment_align: 8
    .kernarg_segment_size: 120
    .language:       OpenCL C
    .language_version:
      - 2
      - 0
    .max_flat_workgroup_size: 256
    .name:           _Z5k0_lnPKfS0_S0_S0_PDF16_S1_S1_S0_S0_S0_S0_S0_S0_S0_S1_
    .private_segment_fixed_size: 0
    .sgpr_count:     31
    .sgpr_spill_count: 0
    .symbol:         _Z5k0_lnPKfS0_S0_S0_PDF16_S1_S1_S0_S0_S0_S0_S0_S0_S0_S1_.kd
    .uniform_work_group_size: 1
    .uses_dynamic_stack: false
    .vgpr_count:     96
    .vgpr_spill_count: 0
    .wavefront_size: 64
  - .agpr_count:     0
    .args:
      - .actual_access:  read_only
        .address_space:  global
        .offset:         0
        .size:           8
        .value_kind:     global_buffer
      - .actual_access:  read_only
        .address_space:  global
        .offset:         8
        .size:           8
        .value_kind:     global_buffer
      - .actual_access:  read_only
        .address_space:  global
        .offset:         16
        .size:           8
        .value_kind:     global_buffer
      - .actual_access:  read_only
        .address_space:  global
        .offset:         24
        .size:           8
        .value_kind:     global_buffer
      - .actual_access:  read_only
        .address_space:  global
        .offset:         32
        .size:           8
        .value_kind:     global_buffer
      - .actual_access:  write_only
        .address_space:  global
        .offset:         40
        .size:           8
        .value_kind:     global_buffer
    .group_segment_fixed_size: 149200
    .kernarg_segment_align: 8
    .kernarg_segment_size: 48
    .language:       OpenCL C
    .language_version:
      - 2
      - 0
    .max_flat_workgroup_size: 1024
    .name:           _Z6k1_mfePKDF16_PKfS2_S2_S2_PDF16_
    .private_segment_fixed_size: 0
    .sgpr_count:     30
    .sgpr_spill_count: 0
    .symbol:         _Z6k1_mfePKDF16_PKfS2_S2_S2_PDF16_.kd
    .uniform_work_group_size: 1
    .uses_dynamic_stack: false
    .vgpr_count:     50
    .vgpr_spill_count: 0
    .wavefront_size: 64
  - .agpr_count:     0
    .args:
      - .actual_access:  read_only
        .address_space:  global
        .offset:         0
        .size:           8
        .value_kind:     global_buffer
      - .actual_access:  read_only
        .address_space:  global
        .offset:         8
        .size:           8
        .value_kind:     global_buffer
      - .actual_access:  read_only
        .address_space:  global
        .offset:         16
        .size:           8
        .value_kind:     global_buffer
      - .actual_access:  read_only
        .address_space:  global
        .offset:         24
        .size:           8
        .value_kind:     global_buffer
      - .actual_access:  write_only
        .address_space:  global
        .offset:         32
        .size:           8
        .value_kind:     global_buffer
      - .actual_access:  write_only
        .address_space:  global
        .offset:         40
        .size:           8
        .value_kind:     global_buffer
      - .actual_access:  write_only
        .address_space:  global
        .offset:         48
        .size:           8
        .value_kind:     global_buffer
    .group_segment_fixed_size: 71424
    .kernarg_segment_align: 8
    .kernarg_segment_size: 56
    .language:       OpenCL C
    .language_version:
      - 2
      - 0
    .max_flat_workgroup_size: 512
    .name:           _Z5k2_kvPKDF16_S0_S0_S0_PDF16_S1_Pf
    .private_segment_fixed_size: 0
    .sgpr_count:     33
    .sgpr_spill_count: 0
    .symbol:         _Z5k2_kvPKDF16_S0_S0_S0_PDF16_S1_Pf.kd
    .uniform_work_group_size: 1
    .uses_dynamic_stack: false
    .vgpr_count:     114
    .vgpr_spill_count: 0
    .wavefront_size: 64
  - .agpr_count:     0
    .args:
      - .actual_access:  read_only
        .address_space:  global
        .offset:         0
        .size:           8
        .value_kind:     global_buffer
      - .actual_access:  write_only
        .address_space:  global
        .offset:         8
        .size:           8
        .value_kind:     global_buffer
    .group_segment_fixed_size: 1024
    .kernarg_segment_align: 8
    .kernarg_segment_size: 16
    .language:       OpenCL C
    .language_version:
      - 2
      - 0
    .max_flat_workgroup_size: 256
    .name:           _Z9k3_reducePKfPf
    .private_segment_fixed_size: 0
    .sgpr_count:     13
    .sgpr_spill_count: 0
    .symbol:         _Z9k3_reducePKfPf.kd
    .uniform_work_group_size: 1
    .uses_dynamic_stack: false
    .vgpr_count:     50
    .vgpr_spill_count: 0
    .wavefront_size: 64
  - .agpr_count:     0
    .args:
      - .actual_access:  read_only
        .address_space:  global
        .offset:         0
        .size:           8
        .value_kind:     global_buffer
      - .actual_access:  read_only
        .address_space:  global
        .offset:         8
        .size:           8
        .value_kind:     global_buffer
      - .actual_access:  read_only
        .address_space:  global
        .offset:         16
        .size:           8
        .value_kind:     global_buffer
      - .actual_access:  read_only
        .address_space:  global
        .offset:         24
        .size:           8
        .value_kind:     global_buffer
      - .actual_access:  read_only
        .address_space:  global
        .offset:         32
        .size:           8
        .value_kind:     global_buffer
      - .actual_access:  read_only
        .address_space:  global
        .offset:         40
        .size:           8
        .value_kind:     global_buffer
      - .actual_access:  read_only
        .address_space:  global
        .offset:         48
        .size:           8
        .value_kind:     global_buffer
      - .actual_access:  read_only
        .address_space:  global
        .offset:         56
        .size:           8
        .value_kind:     global_buffer
      - .actual_access:  write_only
        .address_space:  global
        .offset:         64
        .size:           8
        .value_kind:     global_buffer
    .group_segment_fixed_size: 74752
    .kernarg_segment_align: 8
    .kernarg_segment_size: 72
    .language:       OpenCL C
    .language_version:
      - 2
      - 0
    .max_flat_workgroup_size: 512
    .name:           _Z8k4_fusedPKfPKDF16_S2_S0_S0_S2_S0_S0_Pf
    .private_segment_fixed_size: 0
    .sgpr_count:     108
    .sgpr_spill_count: 0
    .symbol:         _Z8k4_fusedPKfPKDF16_S2_S0_S0_S2_S0_S0_Pf.kd
    .uniform_work_group_size: 1
    .uses_dynamic_stack: false
    .vgpr_count:     128
    .vgpr_spill_count: 0
    .wavefront_size: 64
